# grid-barrier poll interval shortened (s_sleep 10 to 2) on top of the early-issue + rewritten topic loop version
# baseline (speedup 1.0000x reference)
.LBB1_26:
	s_or_b64 exec, exec, s[12:13]
	v_cndmask_b32_e64 v74, 0, 1, s[16:17]
	v_cmp_ne_u32_e32 vcc, 0, v74
	s_cmp_eq_u64 vcc, exec
	s_cbranch_scc1 .LBB1_23
	s_mov_b64 s[16:17], -1
	s_sleep 2
	s_and_saveexec_b64 s[12:13], s[2:3]
	s_cbranch_execz .LBB1_29
	global_load_dword v74, v[66:67], off sc1
	s_waitcnt vmcnt(0)
	v_cmp_lt_u32_e32 vcc, 31, v74
	s_orn2_b64 s[16:17], vcc, exec

.LBB1_38:
	s_or_b64 exec, exec, s[12:13]
	v_cndmask_b32_e64 v74, 0, 1, s[16:17]
	v_cmp_ne_u32_e32 vcc, 0, v74
	s_cmp_eq_u64 vcc, exec
	s_cbranch_scc1 .LBB1_23
	s_add_i32 s19, s19, 5
	s_cmp_gt_u32 s19, 0x3ffffb
	s_cselect_b64 s[6:7], -1, 0
	s_sleep 2
	s_branch .LBB1_23
